# speedup vs baseline: 1.0049x; 1.0049x over previous
.LBB5_9:
	ds_read_b128 v[168:171], v165
	ds_read_b128 v[172:175], v165 offset:1024
	ds_read_b128 v[176:179], v165 offset:2048
	ds_read_b128 v[192:195], v165 offset:3072
	s_mov_b32 m0, s80
	s_add_u32 s100, s96, s0
	s_addc_u32 s101, s97, s1
	global_load_lds_dwordx4 v254, s[100:101]
	s_mov_b32 m0, s81
	s_nop 0
	global_load_lds_dwordx4 v255, s[100:101]
	ds_read_b128 v[196:199], v150
	ds_read_b128 v[200:203], v150 offset:1024
	ds_read_b128 v[204:207], v149
	ds_read_b128 v[208:211], v149 offset:1024
	ds_read_b128 v[212:215], v148
	ds_read_b128 v[216:219], v148 offset:1024
	ds_read_b128 v[220:223], v147
	ds_read_b128 v[224:227], v147 offset:1024
	s_waitcnt lgkmcnt(8)
	s_barrier
	s_waitcnt lgkmcnt(0)
	s_setprio 1
	s_waitcnt lgkmcnt(0)
	v_mfma_f32_16x16x32_f16 v[126:129], v[168:171], v[196:199], v[126:129]
	v_mfma_f32_16x16x32_f16 v[122:125], v[176:179], v[196:199], v[122:125]
	v_mfma_f32_16x16x32_f16 v[118:121], v[168:171], v[204:207], v[118:121]
	v_mfma_f32_16x16x32_f16 v[114:117], v[176:179], v[204:207], v[114:117]
	v_mfma_f32_16x16x32_f16 v[110:113], v[168:171], v[212:215], v[110:113]
	v_mfma_f32_16x16x32_f16 v[106:109], v[176:179], v[212:215], v[106:109]
	v_mfma_f32_16x16x32_f16 v[102:105], v[168:171], v[220:223], v[102:105]
	v_mfma_f32_16x16x32_f16 v[98:101], v[176:179], v[220:223], v[98:101]
	v_mfma_f32_16x16x32_f16 v[126:129], v[172:175], v[200:203], v[126:129]
	v_mfma_f32_16x16x32_f16 v[122:125], v[192:195], v[200:203], v[122:125]
	v_mfma_f32_16x16x32_f16 v[118:121], v[172:175], v[208:211], v[118:121]
	v_mfma_f32_16x16x32_f16 v[114:117], v[192:195], v[208:211], v[114:117]
	v_mfma_f32_16x16x32_f16 v[110:113], v[172:175], v[216:219], v[110:113]
	v_mfma_f32_16x16x32_f16 v[106:109], v[192:195], v[216:219], v[106:109]
	v_mfma_f32_16x16x32_f16 v[102:105], v[172:175], v[224:227], v[102:105]
	v_mfma_f32_16x16x32_f16 v[98:101], v[192:195], v[224:227], v[98:101]
	s_setprio 0
	s_barrier
	s_mov_b32 m0, s82
	ds_read_b128 v[228:231], v163
	ds_read_b128 v[232:235], v163 offset:1024
	ds_read_b128 v[236:239], v163 offset:2048
	ds_read_b128 v[240:243], v163 offset:3072
	s_add_u32 s100, s98, s28
	s_addc_u32 s101, s99, s29
	global_load_lds_dwordx4 v254, s[100:101]
	s_mov_b32 m0, s83
	s_nop 0
	global_load_lds_dwordx4 v255, s[100:101]
	s_barrier
	s_waitcnt lgkmcnt(0)
	s_setprio 1
	s_waitcnt lgkmcnt(0)
	v_mfma_f32_16x16x32_f16 v[94:97], v[228:231], v[196:199], v[94:97]
	v_mfma_f32_16x16x32_f16 v[90:93], v[236:239], v[196:199], v[90:93]
	v_mfma_f32_16x16x32_f16 v[86:89], v[228:231], v[204:207], v[86:89]
	v_mfma_f32_16x16x32_f16 v[82:85], v[236:239], v[204:207], v[82:85]
	v_mfma_f32_16x16x32_f16 v[78:81], v[228:231], v[212:215], v[78:81]
	v_mfma_f32_16x16x32_f16 v[74:77], v[236:239], v[212:215], v[74:77]
	v_mfma_f32_16x16x32_f16 v[70:73], v[228:231], v[220:223], v[70:73]
	v_mfma_f32_16x16x32_f16 v[66:69], v[236:239], v[220:223], v[66:69]
	v_mfma_f32_16x16x32_f16 v[94:97], v[232:235], v[200:203], v[94:97]
	v_mfma_f32_16x16x32_f16 v[90:93], v[240:243], v[200:203], v[90:93]
	v_mfma_f32_16x16x32_f16 v[86:89], v[232:235], v[208:211], v[86:89]
	v_mfma_f32_16x16x32_f16 v[82:85], v[240:243], v[208:211], v[82:85]
	v_mfma_f32_16x16x32_f16 v[78:81], v[232:235], v[216:219], v[78:81]
	v_mfma_f32_16x16x32_f16 v[74:77], v[240:243], v[216:219], v[74:77]
	v_mfma_f32_16x16x32_f16 v[70:73], v[232:235], v[224:227], v[70:73]
	v_mfma_f32_16x16x32_f16 v[66:69], v[240:243], v[224:227], v[66:69]
	s_setprio 0
	s_mov_b32 m0, s84
	s_barrier
	ds_read_b128 v[196:199], v150 offset:16384
	ds_read_b128 v[200:203], v150 offset:17408
	ds_read_b128 v[204:207], v149 offset:16384
	ds_read_b128 v[208:211], v149 offset:17408
	ds_read_b128 v[212:215], v148 offset:16384
	ds_read_b128 v[216:219], v148 offset:17408
	ds_read_b128 v[220:223], v147 offset:16384
	ds_read_b128 v[224:227], v147 offset:17408
	s_add_u32 s100, s96, s28
	s_addc_u32 s101, s97, s29
	global_load_lds_dwordx4 v254, s[100:101]
	s_mov_b32 m0, s85
	s_nop 0
	global_load_lds_dwordx4 v255, s[100:101]
	s_barrier
	s_waitcnt lgkmcnt(0)
	s_setprio 1
	s_waitcnt lgkmcnt(0)
	v_mfma_f32_16x16x32_f16 v[62:65], v[168:171], v[196:199], v[62:65]
	v_mfma_f32_16x16x32_f16 v[58:61], v[176:179], v[196:199], v[58:61]
	v_mfma_f32_16x16x32_f16 v[54:57], v[168:171], v[204:207], v[54:57]
	v_mfma_f32_16x16x32_f16 v[50:53], v[176:179], v[204:207], v[50:53]
	v_mfma_f32_16x16x32_f16 v[46:49], v[168:171], v[212:215], v[46:49]
	v_mfma_f32_16x16x32_f16 v[42:45], v[176:179], v[212:215], v[42:45]
	v_mfma_f32_16x16x32_f16 v[38:41], v[168:171], v[220:223], v[38:41]
	v_mfma_f32_16x16x32_f16 v[34:37], v[176:179], v[220:223], v[34:37]
	v_mfma_f32_16x16x32_f16 v[62:65], v[172:175], v[200:203], v[62:65]
	v_mfma_f32_16x16x32_f16 v[58:61], v[192:195], v[200:203], v[58:61]
	v_mfma_f32_16x16x32_f16 v[54:57], v[172:175], v[208:211], v[54:57]
	v_mfma_f32_16x16x32_f16 v[50:53], v[192:195], v[208:211], v[50:53]
	v_mfma_f32_16x16x32_f16 v[46:49], v[172:175], v[216:219], v[46:49]
	v_mfma_f32_16x16x32_f16 v[42:45], v[192:195], v[216:219], v[42:45]
	v_mfma_f32_16x16x32_f16 v[38:41], v[172:175], v[224:227], v[38:41]
	v_mfma_f32_16x16x32_f16 v[34:37], v[192:195], v[224:227], v[34:37]
	s_setprio 0
	s_barrier
	s_mov_b32 m0, s86
	s_add_u32 s100, s98, s30
	s_addc_u32 s101, s99, s31
	global_load_lds_dwordx4 v254, s[100:101]
	s_mov_b32 m0, s87
	s_nop 0
	global_load_lds_dwordx4 v255, s[100:101]
	s_waitcnt vmcnt(6)
	s_barrier
	s_setprio 1
	v_mfma_f32_16x16x32_f16 v[30:33], v[228:231], v[196:199], v[30:33]
	v_mfma_f32_16x16x32_f16 v[26:29], v[236:239], v[196:199], v[26:29]
	v_mfma_f32_16x16x32_f16 v[22:25], v[228:231], v[204:207], v[22:25]
	v_mfma_f32_16x16x32_f16 v[18:21], v[236:239], v[204:207], v[18:21]
	v_mfma_f32_16x16x32_f16 v[14:17], v[228:231], v[212:215], v[14:17]
	v_mfma_f32_16x16x32_f16 v[10:13], v[236:239], v[212:215], v[10:13]
	v_mfma_f32_16x16x32_f16 v[6:9], v[228:231], v[220:223], v[6:9]
	v_mfma_f32_16x16x32_f16 v[2:5], v[236:239], v[220:223], v[2:5]
	v_mfma_f32_16x16x32_f16 v[30:33], v[232:235], v[200:203], v[30:33]
	v_mfma_f32_16x16x32_f16 v[26:29], v[240:243], v[200:203], v[26:29]
	v_mfma_f32_16x16x32_f16 v[22:25], v[232:235], v[208:211], v[22:25]
	v_mfma_f32_16x16x32_f16 v[18:21], v[240:243], v[208:211], v[18:21]
	v_mfma_f32_16x16x32_f16 v[14:17], v[232:235], v[216:219], v[14:17]
	v_mfma_f32_16x16x32_f16 v[10:13], v[240:243], v[216:219], v[10:13]
	v_mfma_f32_16x16x32_f16 v[6:9], v[232:235], v[224:227], v[6:9]
	v_mfma_f32_16x16x32_f16 v[2:5], v[240:243], v[224:227], v[2:5]
	s_setprio 0
	s_barrier
	ds_read_b128 v[168:171], v133
	ds_read_b128 v[172:175], v133 offset:1024
	ds_read_b128 v[176:179], v133 offset:2048
	ds_read_b128 v[192:195], v133 offset:3072
	s_mov_b32 m0, s88
	ds_read_b128 v[196:199], v150 offset:32768
	ds_read_b128 v[200:203], v150 offset:33792
	ds_read_b128 v[204:207], v149 offset:32768
	ds_read_b128 v[208:211], v149 offset:33792
	ds_read_b128 v[212:215], v148 offset:32768
	ds_read_b128 v[216:219], v148 offset:33792
	ds_read_b128 v[220:223], v147 offset:32768
	ds_read_b128 v[224:227], v147 offset:33792
	s_add_u32 s100, s96, s30
	s_addc_u32 s101, s97, s31
	global_load_lds_dwordx4 v254, s[100:101]
	s_mov_b32 m0, s89
	s_nop 0
	global_load_lds_dwordx4 v255, s[100:101]
	s_waitcnt lgkmcnt(8)
	s_barrier
	s_waitcnt lgkmcnt(0)
	s_setprio 1
	s_waitcnt lgkmcnt(0)
	v_mfma_f32_16x16x32_f16 v[126:129], v[168:171], v[196:199], v[126:129]
	v_mfma_f32_16x16x32_f16 v[122:125], v[176:179], v[196:199], v[122:125]
	v_mfma_f32_16x16x32_f16 v[118:121], v[168:171], v[204:207], v[118:121]
	v_mfma_f32_16x16x32_f16 v[114:117], v[176:179], v[204:207], v[114:117]
	v_mfma_f32_16x16x32_f16 v[110:113], v[168:171], v[212:215], v[110:113]
	v_mfma_f32_16x16x32_f16 v[106:109], v[176:179], v[212:215], v[106:109]
	v_mfma_f32_16x16x32_f16 v[102:105], v[168:171], v[220:223], v[102:105]
	v_mfma_f32_16x16x32_f16 v[98:101], v[176:179], v[220:223], v[98:101]
	v_mfma_f32_16x16x32_f16 v[126:129], v[172:175], v[200:203], v[126:129]
	v_mfma_f32_16x16x32_f16 v[122:125], v[192:195], v[200:203], v[122:125]
	v_mfma_f32_16x16x32_f16 v[118:121], v[172:175], v[208:211], v[118:121]
	v_mfma_f32_16x16x32_f16 v[114:117], v[192:195], v[208:211], v[114:117]
	v_mfma_f32_16x16x32_f16 v[110:113], v[172:175], v[216:219], v[110:113]
	v_mfma_f32_16x16x32_f16 v[106:109], v[192:195], v[216:219], v[106:109]
	v_mfma_f32_16x16x32_f16 v[102:105], v[172:175], v[224:227], v[102:105]
	v_mfma_f32_16x16x32_f16 v[98:101], v[192:195], v[224:227], v[98:101]
	s_setprio 0
	s_barrier
	s_mov_b32 m0, s90
	ds_read_b128 v[228:231], v131
	ds_read_b128 v[232:235], v131 offset:1024
	ds_read_b128 v[236:239], v131 offset:2048
	ds_read_b128 v[240:243], v131 offset:3072
	s_add_u32 s100, s98, s52
	s_addc_u32 s101, s99, s53
	global_load_lds_dwordx4 v254, s[100:101]
	s_mov_b32 m0, s91
	s_nop 0
	global_load_lds_dwordx4 v255, s[100:101]
	s_barrier
	s_waitcnt lgkmcnt(0)
	s_setprio 1
	s_waitcnt lgkmcnt(0)
	v_mfma_f32_16x16x32_f16 v[94:97], v[228:231], v[196:199], v[94:97]
	v_mfma_f32_16x16x32_f16 v[90:93], v[236:239], v[196:199], v[90:93]
	v_mfma_f32_16x16x32_f16 v[86:89], v[228:231], v[204:207], v[86:89]
	v_mfma_f32_16x16x32_f16 v[82:85], v[236:239], v[204:207], v[82:85]
	v_mfma_f32_16x16x32_f16 v[78:81], v[228:231], v[212:215], v[78:81]
	v_mfma_f32_16x16x32_f16 v[74:77], v[236:239], v[212:215], v[74:77]
	v_mfma_f32_16x16x32_f16 v[70:73], v[228:231], v[220:223], v[70:73]
	v_mfma_f32_16x16x32_f16 v[66:69], v[236:239], v[220:223], v[66:69]
	v_mfma_f32_16x16x32_f16 v[94:97], v[232:235], v[200:203], v[94:97]
	v_mfma_f32_16x16x32_f16 v[90:93], v[240:243], v[200:203], v[90:93]
	v_mfma_f32_16x16x32_f16 v[86:89], v[232:235], v[208:211], v[86:89]
	v_mfma_f32_16x16x32_f16 v[82:85], v[240:243], v[208:211], v[82:85]
	v_mfma_f32_16x16x32_f16 v[78:81], v[232:235], v[216:219], v[78:81]
	v_mfma_f32_16x16x32_f16 v[74:77], v[240:243], v[216:219], v[74:77]
	v_mfma_f32_16x16x32_f16 v[70:73], v[232:235], v[224:227], v[70:73]
	v_mfma_f32_16x16x32_f16 v[66:69], v[240:243], v[224:227], v[66:69]
	s_setprio 0
	s_mov_b32 m0, s92
	s_barrier
	ds_read_b128 v[196:199], v150 offset:49152
	ds_read_b128 v[200:203], v150 offset:50176
	ds_read_b128 v[204:207], v149 offset:49152
	ds_read_b128 v[208:211], v149 offset:50176
	ds_read_b128 v[212:215], v148 offset:49152
	ds_read_b128 v[216:219], v148 offset:50176
	ds_read_b128 v[220:223], v147 offset:49152
	ds_read_b128 v[224:227], v147 offset:50176
	s_add_u32 s100, s96, s52
	s_addc_u32 s101, s97, s53
	global_load_lds_dwordx4 v254, s[100:101]
	s_mov_b32 m0, s93
	s_nop 0
	global_load_lds_dwordx4 v255, s[100:101]
	s_barrier
	s_waitcnt lgkmcnt(0)
	s_setprio 1
	s_waitcnt lgkmcnt(0)
	v_mfma_f32_16x16x32_f16 v[62:65], v[168:171], v[196:199], v[62:65]
	v_mfma_f32_16x16x32_f16 v[58:61], v[176:179], v[196:199], v[58:61]
	v_mfma_f32_16x16x32_f16 v[54:57], v[168:171], v[204:207], v[54:57]
	v_mfma_f32_16x16x32_f16 v[50:53], v[176:179], v[204:207], v[50:53]
	v_mfma_f32_16x16x32_f16 v[46:49], v[168:171], v[212:215], v[46:49]
	v_mfma_f32_16x16x32_f16 v[42:45], v[176:179], v[212:215], v[42:45]
	v_mfma_f32_16x16x32_f16 v[38:41], v[168:171], v[220:223], v[38:41]
	v_mfma_f32_16x16x32_f16 v[34:37], v[176:179], v[220:223], v[34:37]
	v_mfma_f32_16x16x32_f16 v[62:65], v[172:175], v[200:203], v[62:65]
	v_mfma_f32_16x16x32_f16 v[58:61], v[192:195], v[200:203], v[58:61]
	v_mfma_f32_16x16x32_f16 v[54:57], v[172:175], v[208:211], v[54:57]
	v_mfma_f32_16x16x32_f16 v[50:53], v[192:195], v[208:211], v[50:53]
	v_mfma_f32_16x16x32_f16 v[46:49], v[172:175], v[216:219], v[46:49]
	v_mfma_f32_16x16x32_f16 v[42:45], v[192:195], v[216:219], v[42:45]
	v_mfma_f32_16x16x32_f16 v[38:41], v[172:175], v[224:227], v[38:41]
	v_mfma_f32_16x16x32_f16 v[34:37], v[192:195], v[224:227], v[34:37]
	s_setprio 0
	s_barrier
	s_mov_b32 m0, s94
	s_add_u32 s100, s98, s54
	s_addc_u32 s101, s99, s55
	global_load_lds_dwordx4 v254, s[100:101]
	s_mov_b32 m0, s95
	s_nop 0
	global_load_lds_dwordx4 v255, s[100:101]
	s_waitcnt vmcnt(6)
	s_barrier
	s_setprio 1
	v_mfma_f32_16x16x32_f16 v[30:33], v[228:231], v[196:199], v[30:33]
	v_mfma_f32_16x16x32_f16 v[26:29], v[236:239], v[196:199], v[26:29]
	v_mfma_f32_16x16x32_f16 v[22:25], v[228:231], v[204:207], v[22:25]
	v_mfma_f32_16x16x32_f16 v[18:21], v[236:239], v[204:207], v[18:21]
	v_mfma_f32_16x16x32_f16 v[14:17], v[228:231], v[212:215], v[14:17]
	v_mfma_f32_16x16x32_f16 v[10:13], v[236:239], v[212:215], v[10:13]
	v_mfma_f32_16x16x32_f16 v[6:9], v[228:231], v[220:223], v[6:9]
	v_mfma_f32_16x16x32_f16 v[2:5], v[236:239], v[220:223], v[2:5]
	v_mfma_f32_16x16x32_f16 v[30:33], v[232:235], v[200:203], v[30:33]
	v_mfma_f32_16x16x32_f16 v[26:29], v[240:243], v[200:203], v[26:29]
	v_mfma_f32_16x16x32_f16 v[22:25], v[232:235], v[208:211], v[22:25]
	v_mfma_f32_16x16x32_f16 v[18:21], v[240:243], v[208:211], v[18:21]
	v_mfma_f32_16x16x32_f16 v[14:17], v[232:235], v[216:219], v[14:17]
	v_mfma_f32_16x16x32_f16 v[10:13], v[240:243], v[216:219], v[10:13]
	v_mfma_f32_16x16x32_f16 v[6:9], v[232:235], v[224:227], v[6:9]
	v_mfma_f32_16x16x32_f16 v[2:5], v[240:243], v[224:227], v[2:5]
	s_setprio 0
	s_add_i32 s35, s35, 2
	s_add_u32 s2, s2, 0x100
	s_addc_u32 s3, s3, 0
	s_add_u32 s96, s96, 0x100
	s_addc_u32 s97, s97, 0
	s_add_u32 s98, s98, 0x100
	s_addc_u32 s99, s99, 0
	s_cmp_lt_u32 s35, 28
	s_barrier
	s_cbranch_scc1 .LBB5_9
	v_add_u32_e32 v143, 0xc000, v142
	s_add_u32 s0, s50, 0x80f80
	v_readfirstlane_b32 s2, v143
	s_addc_u32 s1, s51, 0
	s_mov_b32 m0, s2
	ds_read_b128 v[134:137], v165
	ds_read_b128 v[138:141], v165 offset:1024
	ds_read_b128 v[154:157], v165 offset:2048
	ds_read_b128 v[158:161], v165 offset:3072
	global_load_lds_dwordx4 v130, s[0:1]
	v_add_u32_e32 v130, 0xe000, v142
	s_nop 0
	v_readfirstlane_b32 s2, v130
	s_mov_b32 m0, s2
	s_nop 0
	global_load_lds_dwordx4 v132, s[0:1]
	ds_read_b128 v[142:145], v150
	ds_read_b128 v[166:169], v150 offset:1024
	ds_read_b128 v[170:173], v149
	ds_read_b128 v[174:177], v149 offset:1024
	ds_read_b128 v[192:195], v148
	ds_read_b128 v[196:199], v148 offset:1024
	ds_read_b128 v[200:203], v147
	ds_read_b128 v[204:207], v147 offset:1024
	s_barrier
	s_waitcnt lgkmcnt(0)
	s_setprio 1
	s_waitcnt lgkmcnt(0)
	v_mfma_f32_16x16x32_f16 v[126:129], v[134:137], v[142:145], v[126:129]
	v_mfma_f32_16x16x32_f16 v[122:125], v[154:157], v[142:145], v[122:125]
	v_mfma_f32_16x16x32_f16 v[118:121], v[134:137], v[170:173], v[118:121]
	v_mfma_f32_16x16x32_f16 v[114:117], v[154:157], v[170:173], v[114:117]
	v_mfma_f32_16x16x32_f16 v[110:113], v[134:137], v[192:195], v[110:113]
	v_mfma_f32_16x16x32_f16 v[106:109], v[154:157], v[192:195], v[106:109]
	v_mfma_f32_16x16x32_f16 v[102:105], v[134:137], v[200:203], v[102:105]
	v_mfma_f32_16x16x32_f16 v[98:101], v[154:157], v[200:203], v[98:101]
	v_mfma_f32_16x16x32_f16 v[126:129], v[138:141], v[166:169], v[126:129]
	v_mfma_f32_16x16x32_f16 v[122:125], v[158:161], v[166:169], v[122:125]
	v_mfma_f32_16x16x32_f16 v[118:121], v[138:141], v[174:177], v[118:121]
	v_mfma_f32_16x16x32_f16 v[114:117], v[158:161], v[174:177], v[114:117]
	v_mfma_f32_16x16x32_f16 v[110:113], v[138:141], v[196:199], v[110:113]
	v_mfma_f32_16x16x32_f16 v[106:109], v[158:161], v[196:199], v[106:109]
	v_mfma_f32_16x16x32_f16 v[102:105], v[138:141], v[204:207], v[102:105]
	v_mfma_f32_16x16x32_f16 v[98:101], v[158:161], v[204:207], v[98:101]
	s_setprio 0
	s_barrier
	ds_read_b128 v[208:211], v163
	ds_read_b128 v[212:215], v163 offset:1024
	ds_read_b128 v[216:219], v163 offset:2048
	ds_read_b128 v[220:223], v163 offset:3072
	s_barrier
	s_waitcnt lgkmcnt(0)
	s_setprio 1
	s_waitcnt lgkmcnt(0)
	v_mfma_f32_16x16x32_f16 v[86:89], v[208:211], v[170:173], v[86:89]
	v_mfma_f32_16x16x32_f16 v[82:85], v[216:219], v[170:173], v[82:85]
	v_mfma_f32_16x16x32_f16 v[78:81], v[208:211], v[192:195], v[78:81]
	v_mfma_f32_16x16x32_f16 v[74:77], v[216:219], v[192:195], v[74:77]
	v_mfma_f32_16x16x32_f16 v[70:73], v[208:211], v[200:203], v[70:73]
	v_mfma_f32_16x16x32_f16 v[66:69], v[216:219], v[200:203], v[66:69]
	v_mfma_f32_16x16x32_f16 v[94:97], v[208:211], v[142:145], v[94:97]
	v_mfma_f32_16x16x32_f16 v[90:93], v[216:219], v[142:145], v[90:93]
	v_mfma_f32_16x16x32_f16 v[86:89], v[212:215], v[174:177], v[86:89]
	v_mfma_f32_16x16x32_f16 v[82:85], v[220:223], v[174:177], v[82:85]
	v_mfma_f32_16x16x32_f16 v[78:81], v[212:215], v[196:199], v[78:81]
	v_mfma_f32_16x16x32_f16 v[74:77], v[220:223], v[196:199], v[74:77]
	v_mfma_f32_16x16x32_f16 v[70:73], v[212:215], v[204:207], v[70:73]
	v_mfma_f32_16x16x32_f16 v[66:69], v[220:223], v[204:207], v[66:69]
	v_mfma_f32_16x16x32_f16 v[224:227], v[212:215], v[166:169], v[94:97]
	v_mfma_f32_16x16x32_f16 v[166:169], v[220:223], v[166:169], v[90:93]
	s_setprio 0
	s_barrier
	s_nop 0
	ds_read_b128 v[90:93], v150 offset:16384
	ds_read_b128 v[94:97], v150 offset:17408
	ds_read_b128 v[142:145], v149 offset:16384
	ds_read_b128 v[170:173], v149 offset:17408
	ds_read_b128 v[174:177], v148 offset:16384
	ds_read_b128 v[192:195], v148 offset:17408
	ds_read_b128 v[196:199], v147 offset:16384
	ds_read_b128 v[200:203], v147 offset:17408
	s_waitcnt vmcnt(4)
	s_barrier
	s_waitcnt lgkmcnt(0)
	s_setprio 1
	s_waitcnt lgkmcnt(0)
	v_mfma_f32_16x16x32_f16 v[62:65], v[134:137], v[90:93], v[62:65]
	v_mfma_f32_16x16x32_f16 v[58:61], v[154:157], v[90:93], v[58:61]
	v_mfma_f32_16x16x32_f16 v[54:57], v[134:137], v[142:145], v[54:57]
	v_mfma_f32_16x16x32_f16 v[50:53], v[154:157], v[142:145], v[50:53]
	v_mfma_f32_16x16x32_f16 v[46:49], v[134:137], v[174:177], v[46:49]
	v_mfma_f32_16x16x32_f16 v[42:45], v[154:157], v[174:177], v[42:45]
	v_mfma_f32_16x16x32_f16 v[38:41], v[134:137], v[196:199], v[38:41]
	v_mfma_f32_16x16x32_f16 v[62:65], v[138:141], v[94:97], v[62:65]
	v_mfma_f32_16x16x32_f16 v[58:61], v[158:161], v[94:97], v[58:61]
	v_mfma_f32_16x16x32_f16 v[54:57], v[138:141], v[170:173], v[54:57]
	v_mfma_f32_16x16x32_f16 v[50:53], v[158:161], v[170:173], v[50:53]
	v_mfma_f32_16x16x32_f16 v[46:49], v[138:141], v[192:195], v[46:49]
	v_mfma_f32_16x16x32_f16 v[42:45], v[158:161], v[192:195], v[42:45]
	v_mfma_f32_16x16x32_f16 v[38:41], v[138:141], v[200:203], v[38:41]
	v_mfma_f32_16x16x32_f16 v[34:37], v[154:157], v[196:199], v[34:37]
	v_mfma_f32_16x16x32_f16 v[34:37], v[158:161], v[200:203], v[34:37]
	s_setprio 0
	s_setprio 1
	v_mfma_f32_16x16x32_f16 v[30:33], v[208:211], v[90:93], v[30:33]
	v_mfma_f32_16x16x32_f16 v[6:9], v[208:211], v[196:199], v[6:9]
	v_mfma_f32_16x16x32_f16 v[2:5], v[216:219], v[196:199], v[2:5]
	v_mfma_f32_16x16x32_f16 v[30:33], v[212:215], v[94:97], v[30:33]
	v_mfma_f32_16x16x32_f16 v[26:29], v[216:219], v[90:93], v[26:29]
	v_mfma_f32_16x16x32_f16 v[22:25], v[208:211], v[142:145], v[22:25]
	v_mfma_f32_16x16x32_f16 v[18:21], v[216:219], v[142:145], v[18:21]
	v_mfma_f32_16x16x32_f16 v[14:17], v[208:211], v[174:177], v[14:17]
	v_mfma_f32_16x16x32_f16 v[10:13], v[216:219], v[174:177], v[10:13]
	v_mfma_f32_16x16x32_f16 v[6:9], v[212:215], v[200:203], v[6:9]
	v_mfma_f32_16x16x32_f16 v[2:5], v[220:223], v[200:203], v[2:5]
	v_mfma_f32_16x16x32_f16 v[26:29], v[220:223], v[94:97], v[26:29]
	v_mfma_f32_16x16x32_f16 v[154:157], v[212:215], v[170:173], v[22:25]
	v_mfma_f32_16x16x32_f16 v[18:21], v[220:223], v[170:173], v[18:21]
	v_mfma_f32_16x16x32_f16 v[158:161], v[212:215], v[192:195], v[14:17]
	v_mfma_f32_16x16x32_f16 v[10:13], v[220:223], v[192:195], v[10:13]
	s_setprio 0
	s_barrier
	ds_read_b128 v[14:17], v133
	ds_read_b128 v[22:25], v133 offset:1024
	ds_read_b128 v[170:173], v133 offset:2048
	ds_read_b128 v[174:177], v133 offset:3072
	ds_read_b128 v[192:195], v150 offset:32768
	ds_read_b128 v[196:199], v150 offset:33792
	ds_read_b128 v[200:203], v149 offset:32768
	ds_read_b128 v[204:207], v149 offset:33792
	ds_read_b128 v[208:211], v148 offset:32768
	ds_read_b128 v[212:215], v148 offset:33792
	ds_read_b128 v[216:219], v147 offset:32768
	ds_read_b128 v[220:223], v147 offset:33792
	s_waitcnt vmcnt(2)
	s_barrier
	s_waitcnt lgkmcnt(0)
	s_setprio 1
	s_waitcnt lgkmcnt(0)
	v_mfma_f32_16x16x32_f16 v[90:93], v[14:17], v[192:195], v[126:129]
	v_mfma_f32_16x16x32_f16 v[142:145], v[22:25], v[196:199], v[90:93]
	v_mfma_f32_16x16x32_f16 v[90:93], v[170:173], v[192:195], v[122:125]
	v_mfma_f32_16x16x32_f16 v[138:141], v[174:177], v[196:199], v[90:93]
	v_mfma_f32_16x16x32_f16 v[90:93], v[14:17], v[200:203], v[118:121]
	v_mfma_f32_16x16x32_f16 v[126:129], v[22:25], v[204:207], v[90:93]
	v_mfma_f32_16x16x32_f16 v[90:93], v[170:173], v[200:203], v[114:117]
	v_mfma_f32_16x16x32_f16 v[122:125], v[174:177], v[204:207], v[90:93]
	v_mfma_f32_16x16x32_f16 v[90:93], v[14:17], v[208:211], v[110:113]
	v_mfma_f32_16x16x32_f16 v[110:113], v[22:25], v[212:215], v[90:93]
	v_mfma_f32_16x16x32_f16 v[90:93], v[170:173], v[208:211], v[106:109]
	v_mfma_f32_16x16x32_f16 v[106:109], v[174:177], v[212:215], v[90:93]
	v_mfma_f32_16x16x32_f16 v[90:93], v[14:17], v[216:219], v[102:105]
	v_mfma_f32_16x16x32_f16 v[94:97], v[22:25], v[220:223], v[90:93]
	v_mfma_f32_16x16x32_f16 v[90:93], v[170:173], v[216:219], v[98:101]
	v_mfma_f32_16x16x32_f16 v[90:93], v[174:177], v[220:223], v[90:93]
	s_setprio 0
	s_barrier
	ds_read_b128 v[228:231], v131
	ds_read_b128 v[232:235], v131 offset:1024
	ds_read_b128 v[236:239], v131 offset:2048
	ds_read_b128 v[240:243], v131 offset:3072
	s_waitcnt vmcnt(0)
	s_barrier
	s_waitcnt lgkmcnt(0)
	s_setprio 1
	s_waitcnt lgkmcnt(0)
	v_mfma_f32_16x16x32_f16 v[98:101], v[228:231], v[192:195], v[224:227]
	v_mfma_f32_16x16x32_f16 v[134:137], v[232:235], v[196:199], v[98:101]
	v_mfma_f32_16x16x32_f16 v[98:101], v[236:239], v[192:195], v[166:169]
	v_mfma_f32_16x16x32_f16 v[86:89], v[228:231], v[200:203], v[86:89]
	v_mfma_f32_16x16x32_f16 v[82:85], v[236:239], v[200:203], v[82:85]
	v_mfma_f32_16x16x32_f16 v[78:81], v[228:231], v[208:211], v[78:81]
	v_mfma_f32_16x16x32_f16 v[74:77], v[236:239], v[208:211], v[74:77]
	v_mfma_f32_16x16x32_f16 v[70:73], v[228:231], v[216:219], v[70:73]
	v_mfma_f32_16x16x32_f16 v[66:69], v[236:239], v[216:219], v[66:69]
	v_mfma_f32_16x16x32_f16 v[130:133], v[240:243], v[196:199], v[98:101]
	v_mfma_f32_16x16x32_f16 v[118:121], v[232:235], v[204:207], v[86:89]
	v_mfma_f32_16x16x32_f16 v[114:117], v[240:243], v[204:207], v[82:85]
	v_mfma_f32_16x16x32_f16 v[102:105], v[232:235], v[212:215], v[78:81]
	v_mfma_f32_16x16x32_f16 v[98:101], v[240:243], v[212:215], v[74:77]
	v_mfma_f32_16x16x32_f16 v[86:89], v[232:235], v[220:223], v[70:73]
	v_mfma_f32_16x16x32_f16 v[82:85], v[240:243], v[220:223], v[66:69]
	s_setprio 0
	s_barrier
	s_nop 0
	ds_read_b128 v[66:69], v150 offset:49152
	ds_read_b128 v[166:169], v150 offset:50176
	ds_read_b128 v[192:195], v149 offset:49152
	ds_read_b128 v[196:199], v149 offset:50176
	ds_read_b128 v[200:203], v148 offset:49152
	ds_read_b128 v[148:151], v148 offset:50176
	ds_read_b128 v[204:207], v147 offset:49152
	ds_read_b128 v[208:211], v147 offset:50176
	s_barrier
	s_waitcnt lgkmcnt(0)
	s_setprio 1
	s_waitcnt lgkmcnt(0)
	v_mfma_f32_16x16x32_f16 v[62:65], v[14:17], v[66:69], v[62:65]
	v_mfma_f32_16x16x32_f16 v[54:57], v[14:17], v[192:195], v[54:57]
	v_mfma_f32_16x16x32_f16 v[46:49], v[14:17], v[200:203], v[46:49]
	v_mfma_f32_16x16x32_f16 v[14:17], v[14:17], v[204:207], v[38:41]
	v_mfma_f32_16x16x32_f16 v[78:81], v[22:25], v[166:169], v[62:65]
	v_mfma_f32_16x16x32_f16 v[58:61], v[170:173], v[66:69], v[58:61]
	v_mfma_f32_16x16x32_f16 v[62:65], v[22:25], v[196:199], v[54:57]
	v_mfma_f32_16x16x32_f16 v[50:53], v[170:173], v[192:195], v[50:53]
	v_mfma_f32_16x16x32_f16 v[46:49], v[22:25], v[148:151], v[46:49]
	v_mfma_f32_16x16x32_f16 v[42:45], v[170:173], v[200:203], v[42:45]
	v_mfma_f32_16x16x32_f16 v[22:25], v[22:25], v[208:211], v[14:17]
	v_mfma_f32_16x16x32_f16 v[14:17], v[170:173], v[204:207], v[34:37]
	v_mfma_f32_16x16x32_f16 v[74:77], v[174:177], v[166:169], v[58:61]
	v_mfma_f32_16x16x32_f16 v[58:61], v[174:177], v[196:199], v[50:53]
	v_mfma_f32_16x16x32_f16 v[42:45], v[174:177], v[148:151], v[42:45]
	v_mfma_f32_16x16x32_f16 v[14:17], v[174:177], v[208:211], v[14:17]
	s_setprio 0
	s_setprio 1
	v_mfma_f32_16x16x32_f16 v[26:29], v[236:239], v[66:69], v[26:29]
	v_mfma_f32_16x16x32_f16 v[18:21], v[236:239], v[192:195], v[18:21]
	v_mfma_f32_16x16x32_f16 v[30:33], v[228:231], v[66:69], v[30:33]
	v_mfma_f32_16x16x32_f16 v[66:69], v[240:243], v[166:169], v[26:29]
	v_mfma_f32_16x16x32_f16 v[26:29], v[228:231], v[192:195], v[154:157]
	v_mfma_f32_16x16x32_f16 v[50:53], v[240:243], v[196:199], v[18:21]
	v_mfma_f32_16x16x32_f16 v[18:21], v[228:231], v[200:203], v[158:161]
	v_mfma_f32_16x16x32_f16 v[10:13], v[236:239], v[200:203], v[10:13]
	v_mfma_f32_16x16x32_f16 v[6:9], v[228:231], v[204:207], v[6:9]
	v_mfma_f32_16x16x32_f16 v[2:5], v[236:239], v[204:207], v[2:5]
	v_mfma_f32_16x16x32_f16 v[70:73], v[232:235], v[166:169], v[30:33]
	v_mfma_f32_16x16x32_f16 v[54:57], v[232:235], v[196:199], v[26:29]
	v_mfma_f32_16x16x32_f16 v[38:41], v[232:235], v[148:151], v[18:21]
	v_mfma_f32_16x16x32_f16 v[30:33], v[240:243], v[148:151], v[10:13]
	v_mfma_f32_16x16x32_f16 v[6:9], v[232:235], v[208:211], v[6:9]
	v_mfma_f32_16x16x32_f16 v[2:5], v[240:243], v[208:211], v[2:5]
	s_setprio 0
	s_movk_i32 s0, 0x100
	v_cmp_gt_u32_e32 vcc, s0, v0
	s_barrier
	s_and_saveexec_b64 s[0:1], vcc
	s_cbranch_execz .LBB5_12
	s_barrier
